# combination on v062: EpiKV8 paired dwordx4 stores + unscaled fp8 MFMA in GEMM loops + dequeue atomic wait deferred
# baseline (speedup 1.0000x reference)
.LBB0_951:
	s_ashr_i32 s31, s30, 31
	s_lshl_b64 s[34:35], s[30:31], 17
	s_add_u32 s34, s3, s34
	s_addc_u32 s35, s17, s35
	ds_read_b128 v[14:17], v158
	ds_read_b128 v[18:21], v158 offset:1024
	ds_read_b128 v[30:33], v158 offset:2048
	ds_read_b128 v[34:37], v158 offset:3072
	s_and_b64 s[36:37], s[4:5], exec
	s_cselect_b32 s41, s35, s43
	s_cselect_b32 s40, s34, s42
	s_ashr_i32 s29, s28, 31
	s_lshl_b64 s[36:37], s[28:29], 17
	s_add_u32 s36, s19, s36
	s_addc_u32 s37, s33, s37
	s_and_b64 s[4:5], s[4:5], exec
	s_cselect_b32 s5, s37, s45
	s_cselect_b32 s4, s36, s44
	s_add_u32 s60, s42, 0x10080
	s_addc_u32 s61, s43, 0
	s_add_i32 s65, s39, 0xc000
	v_lshl_add_u64 v[54:55], s[60:61], 0, v[146:147]
	s_mov_b32 m0, s65
	s_add_i32 s29, s39, 0xe000
	ds_read_b128 v[6:9], v159
	ds_read_b128 v[10:13], v159 offset:1024
	ds_read_b128 v[22:25], v159 offset:2048
	ds_read_b128 v[26:29], v159 offset:3072
	ds_read_b128 v[38:41], v159 offset:4096
	ds_read_b128 v[42:45], v159 offset:5120
	ds_read_b128 v[46:49], v159 offset:6144
	ds_read_b128 v[50:53], v159 offset:7168
	global_load_lds_dwordx4 v[54:55], off
	v_lshl_add_u64 v[54:55], s[60:61], 0, v[150:151]
	s_mov_b32 m0, s29
	s_nop 0
	global_load_lds_dwordx4 v[54:55], off
	s_waitcnt lgkmcnt(8)
	s_barrier
	s_waitcnt lgkmcnt(0)
	s_setprio 1
	v_mov_b64_e32 v[124:125], v[4:5]
	v_mov_b64_e32 v[120:121], v[4:5]
	v_mov_b64_e32 v[108:109], v[4:5]
	v_mov_b64_e32 v[104:105], v[4:5]
	v_mov_b64_e32 v[92:93], v[4:5]
	v_mov_b64_e32 v[88:89], v[4:5]
	v_mov_b64_e32 v[60:61], v[4:5]
	v_mov_b64_e32 v[56:57], v[4:5]
	v_mov_b64_e32 v[122:123], v[2:3]
	v_mov_b64_e32 v[118:119], v[2:3]
	v_mov_b64_e32 v[106:107], v[2:3]
	v_mov_b64_e32 v[102:103], v[2:3]
	v_mov_b64_e32 v[90:91], v[2:3]
	v_mov_b64_e32 v[86:87], v[2:3]
	v_mov_b64_e32 v[58:59], v[2:3]
	v_mov_b64_e32 v[54:55], v[2:3]
	s_waitcnt lgkmcnt(0)
	v_mfma_f32_16x16x128_f8f6f4 v[122:125], v[14:21], v[6:13], v[122:125]
	v_mfma_f32_16x16x128_f8f6f4 v[118:121], v[30:37], v[6:13], v[118:121]
	v_mfma_f32_16x16x128_f8f6f4 v[106:109], v[14:21], v[22:29], v[106:109]
	v_mfma_f32_16x16x128_f8f6f4 v[102:105], v[30:37], v[22:29], v[102:105]
	v_mfma_f32_16x16x128_f8f6f4 v[90:93], v[14:21], v[38:45], v[90:93]
	v_mfma_f32_16x16x128_f8f6f4 v[86:89], v[30:37], v[38:45], v[86:89]
	v_mfma_f32_16x16x128_f8f6f4 v[58:61], v[14:21], v[46:53], v[58:61]
	v_mfma_f32_16x16x128_f8f6f4 v[54:57], v[30:37], v[46:53], v[54:57]
	s_setprio 0
	s_barrier
	v_lshl_add_u64 v[140:141], s[44:45], 0, v[148:149]
	s_add_i32 s63, s55, s46
	v_lshl_add_u64 v[62:63], v[140:141], 0, s[6:7]
	s_mov_b32 m0, s63
	v_lshl_add_u64 v[142:143], s[44:45], 0, v[152:153]
	s_add_i32 s31, s63, 0x2000
	ds_read_b128 v[164:167], v161
	ds_read_b128 v[168:171], v161 offset:1024
	ds_read_b128 v[172:175], v161 offset:2048
	ds_read_b128 v[176:179], v161 offset:3072
	global_load_lds_dwordx4 v[62:63], off
	v_lshl_add_u64 v[62:63], v[142:143], 0, s[6:7]
	s_mov_b32 m0, s31
	s_nop 0
	global_load_lds_dwordx4 v[62:63], off
	s_barrier
	s_waitcnt lgkmcnt(0)
	s_setprio 1
	v_mov_b64_e32 v[132:133], v[4:5]
	v_mov_b64_e32 v[128:129], v[4:5]
	v_mov_b64_e32 v[116:117], v[4:5]
	v_mov_b64_e32 v[112:113], v[4:5]
	v_mov_b64_e32 v[100:101], v[4:5]
	v_mov_b64_e32 v[96:97], v[4:5]
	v_mov_b64_e32 v[68:69], v[4:5]
	v_mov_b64_e32 v[64:65], v[4:5]
	v_mov_b64_e32 v[130:131], v[2:3]
	v_mov_b64_e32 v[126:127], v[2:3]
	v_mov_b64_e32 v[114:115], v[2:3]
	v_mov_b64_e32 v[110:111], v[2:3]
	v_mov_b64_e32 v[98:99], v[2:3]
	v_mov_b64_e32 v[94:95], v[2:3]
	v_mov_b64_e32 v[66:67], v[2:3]
	v_mov_b64_e32 v[62:63], v[2:3]
	s_waitcnt lgkmcnt(0)
	v_mfma_f32_16x16x128_f8f6f4 v[130:133], v[164:171], v[6:13], v[130:133]
	v_mfma_f32_16x16x128_f8f6f4 v[126:129], v[172:179], v[6:13], v[126:129]
	v_mfma_f32_16x16x128_f8f6f4 v[114:117], v[164:171], v[22:29], v[114:117]
	v_mfma_f32_16x16x128_f8f6f4 v[110:113], v[172:179], v[22:29], v[110:113]
	v_mfma_f32_16x16x128_f8f6f4 v[98:101], v[164:171], v[38:45], v[98:101]
	v_mfma_f32_16x16x128_f8f6f4 v[94:97], v[172:179], v[38:45], v[94:97]
	v_mfma_f32_16x16x128_f8f6f4 v[66:69], v[164:171], v[46:53], v[66:69]
	v_mfma_f32_16x16x128_f8f6f4 v[62:65], v[172:179], v[46:53], v[62:65]
	s_setprio 0
	v_lshl_add_u64 v[144:145], s[42:43], 0, v[146:147]
	s_mov_b32 m0, s39
	v_lshl_add_u64 v[6:7], v[144:145], 0, s[6:7]
	v_lshl_add_u64 v[154:155], s[42:43], 0, v[150:151]
	s_barrier
	ds_read_b128 v[46:49], v159 offset:16384
	ds_read_b128 v[50:53], v159 offset:17408
	ds_read_b128 v[180:183], v159 offset:18432
	ds_read_b128 v[184:187], v159 offset:19456
	ds_read_b128 v[190:193], v159 offset:20480
	ds_read_b128 v[194:197], v159 offset:21504
	ds_read_b128 v[214:217], v159 offset:22528
	ds_read_b128 v[218:221], v159 offset:23552
	global_load_lds_dwordx4 v[6:7], off
	v_lshl_add_u64 v[6:7], v[154:155], 0, s[6:7]
	s_mov_b32 m0, s48
	s_nop 0
	global_load_lds_dwordx4 v[6:7], off
	s_barrier
	s_waitcnt lgkmcnt(0)
	s_setprio 1
	v_mov_b64_e32 v[76:77], v[4:5]
	v_mov_b64_e32 v[72:73], v[4:5]
	v_mov_b64_e32 v[44:45], v[4:5]
	v_mov_b64_e32 v[40:41], v[4:5]
	v_mov_b64_e32 v[28:29], v[4:5]
	v_mov_b64_e32 v[24:25], v[4:5]
	v_mov_b64_e32 v[12:13], v[4:5]
	v_mov_b64_e32 v[8:9], v[4:5]
	v_mov_b64_e32 v[74:75], v[2:3]
	v_mov_b64_e32 v[70:71], v[2:3]
	v_mov_b64_e32 v[42:43], v[2:3]
	v_mov_b64_e32 v[38:39], v[2:3]
	v_mov_b64_e32 v[26:27], v[2:3]
	v_mov_b64_e32 v[22:23], v[2:3]
	v_mov_b64_e32 v[10:11], v[2:3]
	v_mov_b64_e32 v[6:7], v[2:3]
	s_waitcnt lgkmcnt(0)
	v_mfma_f32_16x16x128_f8f6f4 v[74:77], v[14:21], v[46:53], v[74:77]
	v_mfma_f32_16x16x128_f8f6f4 v[70:73], v[30:37], v[46:53], v[70:73]
	v_mfma_f32_16x16x128_f8f6f4 v[42:45], v[14:21], v[180:187], v[42:45]
	v_mfma_f32_16x16x128_f8f6f4 v[38:41], v[30:37], v[180:187], v[38:41]
	v_mfma_f32_16x16x128_f8f6f4 v[26:29], v[14:21], v[190:197], v[26:29]
	v_mfma_f32_16x16x128_f8f6f4 v[22:25], v[30:37], v[190:197], v[22:25]
	v_mfma_f32_16x16x128_f8f6f4 v[10:13], v[14:21], v[214:221], v[10:13]
	v_mfma_f32_16x16x128_f8f6f4 v[6:9], v[30:37], v[214:221], v[6:9]
	s_setprio 0
	s_barrier
	s_add_u32 s66, s44, 0x10100
	s_addc_u32 s67, s45, 0
	s_add_i32 s61, s56, s46
	v_lshl_add_u64 v[14:15], s[66:67], 0, v[148:149]
	s_mov_b32 m0, s61
	s_add_i32 s60, s61, 0x2000
	global_load_lds_dwordx4 v[14:15], off
	v_lshl_add_u64 v[14:15], s[66:67], 0, v[152:153]
	s_mov_b32 m0, s60
	s_nop 0
	global_load_lds_dwordx4 v[14:15], off
	s_waitcnt vmcnt(6)
	s_barrier
	s_setprio 1
	v_mov_b64_e32 v[84:85], v[4:5]
	v_mov_b64_e32 v[80:81], v[4:5]
	v_mov_b64_e32 v[82:83], v[2:3]
	v_mov_b64_e32 v[78:79], v[2:3]
	v_mfma_f32_16x16x128_f8f6f4 v[82:85], v[164:171], v[46:53], v[82:85]
	v_mfma_f32_16x16x128_f8f6f4 v[78:81], v[172:179], v[46:53], v[78:81]
	v_mov_b64_e32 v[52:53], v[4:5]
	v_mov_b64_e32 v[48:49], v[4:5]
	v_mov_b64_e32 v[36:37], v[4:5]
	v_mov_b64_e32 v[32:33], v[4:5]
	v_mov_b64_e32 v[20:21], v[4:5]
	v_mov_b64_e32 v[16:17], v[4:5]
	v_mov_b64_e32 v[50:51], v[2:3]
	v_mov_b64_e32 v[46:47], v[2:3]
	v_mov_b64_e32 v[34:35], v[2:3]
	v_mov_b64_e32 v[30:31], v[2:3]
	v_mov_b64_e32 v[18:19], v[2:3]
	v_mov_b64_e32 v[14:15], v[2:3]
	v_mfma_f32_16x16x128_f8f6f4 v[50:53], v[164:171], v[180:187], v[50:53]
	v_mfma_f32_16x16x128_f8f6f4 v[46:49], v[172:179], v[180:187], v[46:49]
	v_mfma_f32_16x16x128_f8f6f4 v[34:37], v[164:171], v[190:197], v[34:37]
	v_mfma_f32_16x16x128_f8f6f4 v[30:33], v[172:179], v[190:197], v[30:33]
	v_mfma_f32_16x16x128_f8f6f4 v[18:21], v[164:171], v[214:221], v[18:21]
	v_mfma_f32_16x16x128_f8f6f4 v[14:17], v[172:179], v[214:221], v[14:17]
	s_setprio 0
	s_add_i32 s64, 0, 0x18000
	v_add_u32_e32 v163, s64, v157
	s_barrier
	ds_read_b128 v[166:169], v163
	ds_read_b128 v[170:173], v163 offset:1024
	ds_read_b128 v[174:177], v163 offset:2048
	ds_read_b128 v[178:181], v163 offset:3072
	s_add_u32 s66, s42, 0x10100
	s_addc_u32 s67, s43, 0
	s_mov_b32 m0, s49
	v_lshl_add_u64 v[164:165], s[66:67], 0, v[146:147]
	ds_read_b128 v[190:193], v159 offset:32768
	ds_read_b128 v[194:197], v159 offset:33792
	ds_read_b128 v[214:217], v159 offset:34816
	ds_read_b128 v[218:221], v159 offset:35840
	ds_read_b128 v[222:225], v159 offset:36864
	ds_read_b128 v[226:229], v159 offset:37888
	ds_read_b128 v[230:233], v159 offset:38912
	ds_read_b128 v[234:237], v159 offset:39936
	global_load_lds_dwordx4 v[164:165], off
	v_lshl_add_u64 v[164:165], s[66:67], 0, v[150:151]
	s_mov_b32 m0, s50
	s_nop 0
	global_load_lds_dwordx4 v[164:165], off
	s_waitcnt lgkmcnt(8)
	s_barrier
	s_waitcnt lgkmcnt(0)
	s_setprio 1
	s_waitcnt lgkmcnt(0)
	v_mfma_f32_16x16x128_f8f6f4 v[122:125], v[166:173], v[190:197], v[122:125]
	v_mfma_f32_16x16x128_f8f6f4 v[118:121], v[174:181], v[190:197], v[118:121]
	v_mfma_f32_16x16x128_f8f6f4 v[106:109], v[166:173], v[214:221], v[106:109]
	v_mfma_f32_16x16x128_f8f6f4 v[102:105], v[174:181], v[214:221], v[102:105]
	v_mfma_f32_16x16x128_f8f6f4 v[90:93], v[166:173], v[222:229], v[90:93]
	v_mfma_f32_16x16x128_f8f6f4 v[86:89], v[174:181], v[222:229], v[86:89]
	v_mfma_f32_16x16x128_f8f6f4 v[58:61], v[166:173], v[230:237], v[58:61]
	v_mfma_f32_16x16x128_f8f6f4 v[54:57], v[174:181], v[230:237], v[54:57]
	s_setprio 0
	s_barrier
	s_add_i32 s68, 0, 0x1c000
	s_add_i32 s64, s64, s46
	v_add_u32_e32 v164, s68, v157
	v_lshl_add_u64 v[140:141], v[140:141], 0, s[14:15]
	s_mov_b32 m0, s64
	s_add_i32 s62, s64, 0x2000
	ds_read_b128 v[238:241], v164
	ds_read_b128 v[242:245], v164 offset:1024
	ds_read_b128 v[246:249], v164 offset:2048
	ds_read_b128 v[250:253], v164 offset:3072
	global_load_lds_dwordx4 v[140:141], off
	v_lshl_add_u64 v[140:141], v[142:143], 0, s[14:15]
	s_mov_b32 m0, s62
	s_nop 0
	global_load_lds_dwordx4 v[140:141], off
	s_barrier
	s_waitcnt lgkmcnt(0)
	s_setprio 1
	s_waitcnt lgkmcnt(0)
	v_mfma_f32_16x16x128_f8f6f4 v[130:133], v[238:245], v[190:197], v[130:133]
	v_mfma_f32_16x16x128_f8f6f4 v[126:129], v[246:253], v[190:197], v[126:129]
	v_mfma_f32_16x16x128_f8f6f4 v[114:117], v[238:245], v[214:221], v[114:117]
	v_mfma_f32_16x16x128_f8f6f4 v[110:113], v[246:253], v[214:221], v[110:113]
	v_mfma_f32_16x16x128_f8f6f4 v[98:101], v[238:245], v[222:229], v[98:101]
	v_mfma_f32_16x16x128_f8f6f4 v[94:97], v[246:253], v[222:229], v[94:97]
	v_mfma_f32_16x16x128_f8f6f4 v[66:69], v[238:245], v[230:237], v[66:69]
	v_mfma_f32_16x16x128_f8f6f4 v[62:65], v[246:253], v[230:237], v[62:65]
	s_setprio 0
	s_mov_b32 m0, s51
	v_lshl_add_u64 v[140:141], v[144:145], 0, s[14:15]
	s_barrier
	ds_read_b128 v[190:193], v159 offset:49152
	ds_read_b128 v[194:197], v159 offset:50176
	ds_read_b128 v[214:217], v159 offset:51200
	ds_read_b128 v[218:221], v159 offset:52224
	ds_read_b128 v[222:225], v159 offset:53248
	ds_read_b128 v[226:229], v159 offset:54272
	ds_read_b128 v[230:233], v159 offset:55296
	ds_read_b128 v[234:237], v159 offset:56320
	global_load_lds_dwordx4 v[140:141], off
	v_lshl_add_u64 v[140:141], v[154:155], 0, s[14:15]
	s_mov_b32 m0, s52
	s_nop 0
	global_load_lds_dwordx4 v[140:141], off
	s_barrier
	s_waitcnt lgkmcnt(0)
	s_setprio 1
	s_waitcnt lgkmcnt(0)
	v_mfma_f32_16x16x128_f8f6f4 v[74:77], v[166:173], v[190:197], v[74:77]
	v_mfma_f32_16x16x128_f8f6f4 v[70:73], v[174:181], v[190:197], v[70:73]
	v_mfma_f32_16x16x128_f8f6f4 v[42:45], v[166:173], v[214:221], v[42:45]
	v_mfma_f32_16x16x128_f8f6f4 v[38:41], v[174:181], v[214:221], v[38:41]
	v_mfma_f32_16x16x128_f8f6f4 v[26:29], v[166:173], v[222:229], v[26:29]
	v_mfma_f32_16x16x128_f8f6f4 v[22:25], v[174:181], v[222:229], v[22:25]
	v_mfma_f32_16x16x128_f8f6f4 v[10:13], v[166:173], v[230:237], v[10:13]
	v_mfma_f32_16x16x128_f8f6f4 v[6:9], v[174:181], v[230:237], v[6:9]
	s_setprio 0
	s_barrier
	s_add_u32 s66, s44, 0x10180
	s_addc_u32 s67, s45, 0
	s_add_i32 s45, s68, s46
	v_lshl_add_u64 v[140:141], s[66:67], 0, v[148:149]
	s_mov_b32 m0, s45
	s_add_i32 s44, s45, 0x2000
	global_load_lds_dwordx4 v[140:141], off
	v_lshl_add_u64 v[140:141], s[66:67], 0, v[152:153]
	s_mov_b32 m0, s44
	s_nop 0
	global_load_lds_dwordx4 v[140:141], off
	s_waitcnt vmcnt(6)
	s_barrier
	s_setprio 1
	v_mfma_f32_16x16x128_f8f6f4 v[82:85], v[238:245], v[190:197], v[82:85]
	v_mfma_f32_16x16x128_f8f6f4 v[78:81], v[246:253], v[190:197], v[78:81]
	v_mfma_f32_16x16x128_f8f6f4 v[50:53], v[238:245], v[214:221], v[50:53]
	v_mfma_f32_16x16x128_f8f6f4 v[46:49], v[246:253], v[214:221], v[46:49]
	v_mfma_f32_16x16x128_f8f6f4 v[34:37], v[238:245], v[222:229], v[34:37]
	v_mfma_f32_16x16x128_f8f6f4 v[30:33], v[246:253], v[222:229], v[30:33]
	v_mfma_f32_16x16x128_f8f6f4 v[18:21], v[238:245], v[230:237], v[18:21]
	v_mfma_f32_16x16x128_f8f6f4 v[14:17], v[246:253], v[230:237], v[14:17]
	s_setprio 0
	s_barrier
	ds_read_b128 v[166:169], v158
	ds_read_b128 v[170:173], v158 offset:1024
	ds_read_b128 v[174:177], v158 offset:2048
	ds_read_b128 v[178:181], v158 offset:3072
	s_add_u32 s42, s42, 0x10180
	s_addc_u32 s43, s43, 0
	s_mov_b32 m0, s65
	v_lshl_add_u64 v[140:141], s[42:43], 0, v[146:147]
	ds_read_b128 v[190:193], v159
	ds_read_b128 v[194:197], v159 offset:1024
	ds_read_b128 v[214:217], v159 offset:2048
	ds_read_b128 v[218:221], v159 offset:3072
	ds_read_b128 v[222:225], v159 offset:4096
	ds_read_b128 v[226:229], v159 offset:5120
	ds_read_b128 v[230:233], v159 offset:6144
	ds_read_b128 v[234:237], v159 offset:7168
	global_load_lds_dwordx4 v[140:141], off
	v_lshl_add_u64 v[140:141], s[42:43], 0, v[150:151]
	s_mov_b32 m0, s29
	s_nop 0
	global_load_lds_dwordx4 v[140:141], off
	s_waitcnt lgkmcnt(8)
	s_barrier
	s_waitcnt lgkmcnt(0)
	s_setprio 1
	s_waitcnt lgkmcnt(0)
	v_mfma_f32_16x16x128_f8f6f4 v[122:125], v[166:173], v[190:197], v[122:125]
	v_mfma_f32_16x16x128_f8f6f4 v[118:121], v[174:181], v[190:197], v[118:121]
	v_mfma_f32_16x16x128_f8f6f4 v[106:109], v[166:173], v[214:221], v[106:109]
	v_mfma_f32_16x16x128_f8f6f4 v[102:105], v[174:181], v[214:221], v[102:105]
	v_mfma_f32_16x16x128_f8f6f4 v[90:93], v[166:173], v[222:229], v[90:93]
	v_mfma_f32_16x16x128_f8f6f4 v[86:89], v[174:181], v[222:229], v[86:89]
	v_mfma_f32_16x16x128_f8f6f4 v[58:61], v[166:173], v[230:237], v[58:61]
	v_mfma_f32_16x16x128_f8f6f4 v[54:57], v[174:181], v[230:237], v[54:57]
	s_setprio 0
	s_barrier
	s_mov_b32 m0, s63
	v_lshl_add_u64 v[140:141], s[4:5], 0, v[148:149]
	ds_read_b128 v[238:241], v161
	ds_read_b128 v[242:245], v161 offset:1024
	ds_read_b128 v[246:249], v161 offset:2048
	ds_read_b128 v[250:253], v161 offset:3072
	global_load_lds_dwordx4 v[140:141], off
	v_lshl_add_u64 v[142:143], s[4:5], 0, v[152:153]
	s_mov_b32 m0, s31
	s_nop 0
	global_load_lds_dwordx4 v[142:143], off
	s_barrier
	s_waitcnt lgkmcnt(0)
	s_setprio 1
	s_waitcnt lgkmcnt(0)
	v_mfma_f32_16x16x128_f8f6f4 v[130:133], v[238:245], v[190:197], v[130:133]
	v_mfma_f32_16x16x128_f8f6f4 v[126:129], v[246:253], v[190:197], v[126:129]
	v_mfma_f32_16x16x128_f8f6f4 v[114:117], v[238:245], v[214:221], v[114:117]
	v_mfma_f32_16x16x128_f8f6f4 v[110:113], v[246:253], v[214:221], v[110:113]
	v_mfma_f32_16x16x128_f8f6f4 v[98:101], v[238:245], v[222:229], v[98:101]
	v_mfma_f32_16x16x128_f8f6f4 v[94:97], v[246:253], v[222:229], v[94:97]
	v_mfma_f32_16x16x128_f8f6f4 v[66:69], v[238:245], v[230:237], v[66:69]
	v_mfma_f32_16x16x128_f8f6f4 v[62:65], v[246:253], v[230:237], v[62:65]
	s_setprio 0
	s_mov_b32 m0, s39
	v_lshl_add_u64 v[144:145], s[40:41], 0, v[146:147]
	s_barrier
	ds_read_b128 v[190:193], v159 offset:16384
	ds_read_b128 v[194:197], v159 offset:17408
	ds_read_b128 v[214:217], v159 offset:18432
	ds_read_b128 v[218:221], v159 offset:19456
	ds_read_b128 v[222:225], v159 offset:20480
	ds_read_b128 v[226:229], v159 offset:21504
	ds_read_b128 v[230:233], v159 offset:22528
	ds_read_b128 v[234:237], v159 offset:23552
	global_load_lds_dwordx4 v[144:145], off
	v_lshl_add_u64 v[154:155], s[40:41], 0, v[150:151]
	s_mov_b32 m0, s48
	s_nop 0
	global_load_lds_dwordx4 v[154:155], off
	s_barrier
	s_waitcnt lgkmcnt(0)
	s_setprio 1
	s_waitcnt lgkmcnt(0)
	v_mfma_f32_16x16x128_f8f6f4 v[74:77], v[166:173], v[190:197], v[74:77]
	v_mfma_f32_16x16x128_f8f6f4 v[70:73], v[174:181], v[190:197], v[70:73]
	v_mfma_f32_16x16x128_f8f6f4 v[42:45], v[166:173], v[214:221], v[42:45]
	v_mfma_f32_16x16x128_f8f6f4 v[38:41], v[174:181], v[214:221], v[38:41]
	v_mfma_f32_16x16x128_f8f6f4 v[26:29], v[166:173], v[222:229], v[26:29]
	v_mfma_f32_16x16x128_f8f6f4 v[22:25], v[174:181], v[222:229], v[22:25]
	v_mfma_f32_16x16x128_f8f6f4 v[10:13], v[166:173], v[230:237], v[10:13]
	v_mfma_f32_16x16x128_f8f6f4 v[6:9], v[174:181], v[230:237], v[6:9]
	s_setprio 0
	s_barrier
	s_add_u32 s42, s4, 0x10000
	s_addc_u32 s43, s5, 0
	s_mov_b32 m0, s61
	v_lshl_add_u64 v[166:167], s[42:43], 0, v[148:149]
	global_load_lds_dwordx4 v[166:167], off
	v_lshl_add_u64 v[166:167], s[42:43], 0, v[152:153]
	s_mov_b32 m0, s60
	s_nop 0
	global_load_lds_dwordx4 v[166:167], off
	s_waitcnt vmcnt(6)
	s_barrier
	s_setprio 1
	v_mfma_f32_16x16x128_f8f6f4 v[82:85], v[238:245], v[190:197], v[82:85]
	v_mfma_f32_16x16x128_f8f6f4 v[78:81], v[246:253], v[190:197], v[78:81]
	v_mfma_f32_16x16x128_f8f6f4 v[50:53], v[238:245], v[214:221], v[50:53]
	v_mfma_f32_16x16x128_f8f6f4 v[46:49], v[246:253], v[214:221], v[46:49]
	v_mfma_f32_16x16x128_f8f6f4 v[34:37], v[238:245], v[222:229], v[34:37]
	v_mfma_f32_16x16x128_f8f6f4 v[30:33], v[246:253], v[222:229], v[30:33]
	v_mfma_f32_16x16x128_f8f6f4 v[18:21], v[238:245], v[230:237], v[18:21]
	v_mfma_f32_16x16x128_f8f6f4 v[14:17], v[246:253], v[230:237], v[14:17]
	s_setprio 0
	s_barrier
	ds_read_b128 v[166:169], v163
	ds_read_b128 v[170:173], v163 offset:1024
	ds_read_b128 v[174:177], v163 offset:2048
	ds_read_b128 v[178:181], v163 offset:3072
	s_add_u32 s40, s40, 0x10000
	s_addc_u32 s41, s41, 0
	s_mov_b32 m0, s49
	v_lshl_add_u64 v[182:183], s[40:41], 0, v[146:147]
	ds_read_b128 v[190:193], v159 offset:32768
	ds_read_b128 v[194:197], v159 offset:33792
	ds_read_b128 v[214:217], v159 offset:34816
	ds_read_b128 v[218:221], v159 offset:35840
	ds_read_b128 v[222:225], v159 offset:36864
	ds_read_b128 v[226:229], v159 offset:37888
	ds_read_b128 v[230:233], v159 offset:38912
	ds_read_b128 v[234:237], v159 offset:39936
	global_load_lds_dwordx4 v[182:183], off
	v_lshl_add_u64 v[182:183], s[40:41], 0, v[150:151]
	s_mov_b32 m0, s50
	s_nop 0
	global_load_lds_dwordx4 v[182:183], off
	s_waitcnt lgkmcnt(8)
	s_barrier
	s_waitcnt lgkmcnt(0)
	s_setprio 1
	s_waitcnt lgkmcnt(0)
	v_mfma_f32_16x16x128_f8f6f4 v[122:125], v[166:173], v[190:197], v[122:125]
	v_mfma_f32_16x16x128_f8f6f4 v[118:121], v[174:181], v[190:197], v[118:121]
	v_mfma_f32_16x16x128_f8f6f4 v[106:109], v[166:173], v[214:221], v[106:109]
	v_mfma_f32_16x16x128_f8f6f4 v[102:105], v[174:181], v[214:221], v[102:105]
	v_mfma_f32_16x16x128_f8f6f4 v[90:93], v[166:173], v[222:229], v[90:93]
	v_mfma_f32_16x16x128_f8f6f4 v[86:89], v[174:181], v[222:229], v[86:89]
	v_mfma_f32_16x16x128_f8f6f4 v[58:61], v[166:173], v[230:237], v[58:61]
	v_mfma_f32_16x16x128_f8f6f4 v[54:57], v[174:181], v[230:237], v[54:57]
	s_setprio 0
	s_barrier
	s_mov_b32 m0, s64
	v_lshl_add_u64 v[140:141], v[140:141], 0, s[12:13]
	ds_read_b128 v[238:241], v164
	ds_read_b128 v[242:245], v164 offset:1024
	ds_read_b128 v[246:249], v164 offset:2048
	ds_read_b128 v[250:253], v164 offset:3072
	global_load_lds_dwordx4 v[140:141], off
	v_lshl_add_u64 v[140:141], v[142:143], 0, s[12:13]
	s_mov_b32 m0, s62
	s_nop 0
	global_load_lds_dwordx4 v[140:141], off
	s_barrier
	s_waitcnt lgkmcnt(0)
	s_setprio 1
	s_waitcnt lgkmcnt(0)
	v_mfma_f32_16x16x128_f8f6f4 v[130:133], v[238:245], v[190:197], v[130:133]
	v_mfma_f32_16x16x128_f8f6f4 v[126:129], v[246:253], v[190:197], v[126:129]
	v_mfma_f32_16x16x128_f8f6f4 v[114:117], v[238:245], v[214:221], v[114:117]
	v_mfma_f32_16x16x128_f8f6f4 v[110:113], v[246:253], v[214:221], v[110:113]
	v_mfma_f32_16x16x128_f8f6f4 v[98:101], v[238:245], v[222:229], v[98:101]
	v_mfma_f32_16x16x128_f8f6f4 v[94:97], v[246:253], v[222:229], v[94:97]
	v_mfma_f32_16x16x128_f8f6f4 v[66:69], v[238:245], v[230:237], v[66:69]
	v_mfma_f32_16x16x128_f8f6f4 v[62:65], v[246:253], v[230:237], v[62:65]
	s_setprio 0
	s_mov_b32 m0, s51
	v_lshl_add_u64 v[140:141], v[144:145], 0, s[12:13]
	s_barrier
	ds_read_b128 v[190:193], v159 offset:49152
	ds_read_b128 v[194:197], v159 offset:50176
	ds_read_b128 v[214:217], v159 offset:51200
	ds_read_b128 v[218:221], v159 offset:52224
	ds_read_b128 v[222:225], v159 offset:53248
	ds_read_b128 v[226:229], v159 offset:54272
	ds_read_b128 v[230:233], v159 offset:55296
	ds_read_b128 v[234:237], v159 offset:56320
	global_load_lds_dwordx4 v[140:141], off
	v_lshl_add_u64 v[140:141], v[154:155], 0, s[12:13]
	s_mov_b32 m0, s52
	s_nop 0
	global_load_lds_dwordx4 v[140:141], off
	s_barrier
	s_waitcnt lgkmcnt(0)
	s_setprio 1
	s_waitcnt lgkmcnt(0)
	v_mfma_f32_16x16x128_f8f6f4 v[74:77], v[166:173], v[190:197], v[74:77]
	v_mfma_f32_16x16x128_f8f6f4 v[70:73], v[174:181], v[190:197], v[70:73]
	v_mfma_f32_16x16x128_f8f6f4 v[42:45], v[166:173], v[214:221], v[42:45]
	v_mfma_f32_16x16x128_f8f6f4 v[38:41], v[174:181], v[214:221], v[38:41]
	v_mfma_f32_16x16x128_f8f6f4 v[26:29], v[166:173], v[222:229], v[26:29]
	v_mfma_f32_16x16x128_f8f6f4 v[22:25], v[174:181], v[222:229], v[22:25]
	v_mfma_f32_16x16x128_f8f6f4 v[10:13], v[166:173], v[230:237], v[10:13]
	v_mfma_f32_16x16x128_f8f6f4 v[6:9], v[174:181], v[230:237], v[6:9]
	s_setprio 0
	s_barrier
	s_add_u32 s4, s4, 0x10080
	s_addc_u32 s5, s5, 0
	s_mov_b32 m0, s45
	v_lshl_add_u64 v[140:141], s[4:5], 0, v[148:149]
	global_load_lds_dwordx4 v[140:141], off
	v_lshl_add_u64 v[140:141], s[4:5], 0, v[152:153]
	s_mov_b32 m0, s44
	s_nop 0
	global_load_lds_dwordx4 v[140:141], off
	s_waitcnt vmcnt(6)
	s_barrier
	s_setprio 1
	v_mfma_f32_16x16x128_f8f6f4 v[82:85], v[238:245], v[190:197], v[82:85]
	v_mfma_f32_16x16x128_f8f6f4 v[78:81], v[246:253], v[190:197], v[78:81]
	v_mfma_f32_16x16x128_f8f6f4 v[50:53], v[238:245], v[214:221], v[50:53]
	v_mfma_f32_16x16x128_f8f6f4 v[46:49], v[246:253], v[214:221], v[46:49]
	v_mfma_f32_16x16x128_f8f6f4 v[34:37], v[238:245], v[222:229], v[34:37]
	v_mfma_f32_16x16x128_f8f6f4 v[30:33], v[246:253], v[222:229], v[30:33]
	v_mfma_f32_16x16x128_f8f6f4 v[18:21], v[238:245], v[230:237], v[18:21]
	v_mfma_f32_16x16x128_f8f6f4 v[14:17], v[246:253], v[230:237], v[14:17]
	s_setprio 0
	s_lshl_b32 s4, s59, 7
	s_ashr_i32 s5, s4, 31
	v_lshl_add_u32 v140, s38, 8, v156
	v_bfe_u32 v234, v204, 4, 1
	v_mul_u32_u24_e32 v235, 0x3ff8, v234
	v_add_u32_e32 v232, v134, v235
	v_mov_b32_e32 v233, v135
	s_barrier
	v_mov_b32_e32 v234, v140
	v_ashrrev_i32_e32 v235, 31, v234
	v_lshlrev_b64 v[234:235], 10, v[234:235]
	v_pk_mul_f32 v[122:123], v[122:123], s[16:17] op_sel_hi:[1,0]
	v_pk_mul_f32 v[124:125], v[124:125], s[16:17] op_sel_hi:[1,0]
	v_pk_mul_f32 v[118:119], v[118:119], s[16:17] op_sel_hi:[1,0]
	v_pk_mul_f32 v[120:121], v[120:121], s[16:17] op_sel_hi:[1,0]
	v_pk_mul_f32 v[106:107], v[106:107], s[16:17] op_sel_hi:[1,0]
	v_pk_mul_f32 v[108:109], v[108:109], s[16:17] op_sel_hi:[1,0]
	v_pk_mul_f32 v[102:103], v[102:103], s[16:17] op_sel_hi:[1,0]
	v_pk_mul_f32 v[104:105], v[104:105], s[16:17] op_sel_hi:[1,0]
	v_med3_f32 v122, v122, s57, v162
	v_med3_f32 v123, v123, s57, v162
	v_med3_f32 v124, v124, s57, v162
	v_med3_f32 v125, v125, s57, v162
	v_med3_f32 v118, v118, s57, v162
	v_med3_f32 v119, v119, s57, v162
	v_med3_f32 v120, v120, s57, v162
	v_med3_f32 v121, v121, s57, v162
	v_med3_f32 v106, v106, s57, v162
	v_med3_f32 v107, v107, s57, v162
	v_med3_f32 v108, v108, s57, v162
	v_med3_f32 v109, v109, s57, v162
	v_med3_f32 v102, v102, s57, v162
	v_med3_f32 v103, v103, s57, v162
	v_med3_f32 v104, v104, s57, v162
	v_med3_f32 v105, v105, s57, v162
	v_cvt_pk_fp8_f32 v240, v122, v123
	v_cvt_pk_fp8_f32 v241, v118, v119
	v_cvt_pk_fp8_f32 v242, v106, v107
	v_cvt_pk_fp8_f32 v243, v102, v103
	v_lshl_add_u64 v[236:237], s[10:11], 0, v[234:235]
	v_cvt_pk_fp8_f32 v240, v124, v125 op_sel:[0,0,1]
	v_cvt_pk_fp8_f32 v241, v120, v121 op_sel:[0,0,1]
	v_cvt_pk_fp8_f32 v242, v108, v109 op_sel:[0,0,1]
	v_cvt_pk_fp8_f32 v243, v104, v105 op_sel:[0,0,1]
	v_lshl_add_u64 v[236:237], v[236:237], 0, s[4:5]
	v_lshl_add_u64 v[236:237], v[236:237], 0, v[232:233]
	s_nop 1
	v_permlane16_swap_b32_e32 v240, v242
	v_permlane16_swap_b32_e32 v241, v243
	s_nop 0
	global_store_dwordx4 v[236:237], v[240:243], off
	v_pk_mul_f32 v[130:131], v[130:131], s[18:19] op_sel_hi:[1,0]
	v_pk_mul_f32 v[132:133], v[132:133], s[18:19] op_sel_hi:[1,0]
	v_pk_mul_f32 v[126:127], v[126:127], s[18:19] op_sel_hi:[1,0]
	v_pk_mul_f32 v[128:129], v[128:129], s[18:19] op_sel_hi:[1,0]
	v_pk_mul_f32 v[114:115], v[114:115], s[18:19] op_sel_hi:[1,0]
	v_pk_mul_f32 v[116:117], v[116:117], s[18:19] op_sel_hi:[1,0]
	v_pk_mul_f32 v[110:111], v[110:111], s[18:19] op_sel_hi:[1,0]
	v_pk_mul_f32 v[112:113], v[112:113], s[18:19] op_sel_hi:[1,0]
	v_med3_f32 v130, v130, s57, v162
	v_med3_f32 v131, v131, s57, v162
	v_med3_f32 v132, v132, s57, v162
	v_med3_f32 v133, v133, s57, v162
	v_med3_f32 v126, v126, s57, v162
	v_med3_f32 v127, v127, s57, v162
	v_med3_f32 v128, v128, s57, v162
	v_med3_f32 v129, v129, s57, v162
	v_med3_f32 v114, v114, s57, v162
	v_med3_f32 v115, v115, s57, v162
	v_med3_f32 v116, v116, s57, v162
	v_med3_f32 v117, v117, s57, v162
	v_med3_f32 v110, v110, s57, v162
	v_med3_f32 v111, v111, s57, v162
	v_med3_f32 v112, v112, s57, v162
	v_med3_f32 v113, v113, s57, v162
	v_cvt_pk_fp8_f32 v244, v130, v131
	v_cvt_pk_fp8_f32 v245, v126, v127
	v_cvt_pk_fp8_f32 v246, v114, v115
	v_cvt_pk_fp8_f32 v247, v110, v111
	v_lshl_add_u64 v[238:239], s[8:9], 0, v[234:235]
	v_cvt_pk_fp8_f32 v244, v132, v133 op_sel:[0,0,1]
	v_cvt_pk_fp8_f32 v245, v128, v129 op_sel:[0,0,1]
	v_cvt_pk_fp8_f32 v246, v116, v117 op_sel:[0,0,1]
	v_cvt_pk_fp8_f32 v247, v112, v113 op_sel:[0,0,1]
	v_lshl_add_u64 v[238:239], v[238:239], 0, s[4:5]
	v_lshl_add_u64 v[238:239], v[238:239], 0, v[232:233]
	s_nop 1
	v_permlane16_swap_b32_e32 v244, v246
	v_permlane16_swap_b32_e32 v245, v247
	s_nop 0
	global_store_dwordx4 v[238:239], v[244:247], off
	v_or_b32_e32 v234, 32, v140
	v_ashrrev_i32_e32 v235, 31, v234
	v_lshlrev_b64 v[234:235], 10, v[234:235]
	v_pk_mul_f32 v[90:91], v[90:91], s[16:17] op_sel_hi:[1,0]
	v_pk_mul_f32 v[92:93], v[92:93], s[16:17] op_sel_hi:[1,0]
	v_pk_mul_f32 v[86:87], v[86:87], s[16:17] op_sel_hi:[1,0]
	v_pk_mul_f32 v[88:89], v[88:89], s[16:17] op_sel_hi:[1,0]
	v_pk_mul_f32 v[58:59], v[58:59], s[16:17] op_sel_hi:[1,0]
	v_pk_mul_f32 v[60:61], v[60:61], s[16:17] op_sel_hi:[1,0]
	v_pk_mul_f32 v[54:55], v[54:55], s[16:17] op_sel_hi:[1,0]
	v_pk_mul_f32 v[56:57], v[56:57], s[16:17] op_sel_hi:[1,0]
	v_med3_f32 v90, v90, s57, v162
	v_med3_f32 v91, v91, s57, v162
	v_med3_f32 v92, v92, s57, v162
	v_med3_f32 v93, v93, s57, v162
	v_med3_f32 v86, v86, s57, v162
	v_med3_f32 v87, v87, s57, v162
	v_med3_f32 v88, v88, s57, v162
	v_med3_f32 v89, v89, s57, v162
	v_med3_f32 v58, v58, s57, v162
	v_med3_f32 v59, v59, s57, v162
	v_med3_f32 v60, v60, s57, v162
	v_med3_f32 v61, v61, s57, v162
	v_med3_f32 v54, v54, s57, v162
	v_med3_f32 v55, v55, s57, v162
	v_med3_f32 v56, v56, s57, v162
	v_med3_f32 v57, v57, s57, v162
	v_cvt_pk_fp8_f32 v240, v90, v91
	v_cvt_pk_fp8_f32 v241, v86, v87
	v_cvt_pk_fp8_f32 v242, v58, v59
	v_cvt_pk_fp8_f32 v243, v54, v55
	v_lshl_add_u64 v[236:237], s[10:11], 0, v[234:235]
	v_cvt_pk_fp8_f32 v240, v92, v93 op_sel:[0,0,1]
	v_cvt_pk_fp8_f32 v241, v88, v89 op_sel:[0,0,1]
	v_cvt_pk_fp8_f32 v242, v60, v61 op_sel:[0,0,1]
	v_cvt_pk_fp8_f32 v243, v56, v57 op_sel:[0,0,1]
	v_lshl_add_u64 v[236:237], v[236:237], 0, s[4:5]
	v_lshl_add_u64 v[236:237], v[236:237], 0, v[232:233]
	s_nop 1
	v_permlane16_swap_b32_e32 v240, v242
	v_permlane16_swap_b32_e32 v241, v243
	s_nop 0
	global_store_dwordx4 v[236:237], v[240:243], off
	v_pk_mul_f32 v[98:99], v[98:99], s[18:19] op_sel_hi:[1,0]
	v_pk_mul_f32 v[100:101], v[100:101], s[18:19] op_sel_hi:[1,0]
	v_pk_mul_f32 v[94:95], v[94:95], s[18:19] op_sel_hi:[1,0]
	v_pk_mul_f32 v[96:97], v[96:97], s[18:19] op_sel_hi:[1,0]
	v_pk_mul_f32 v[66:67], v[66:67], s[18:19] op_sel_hi:[1,0]
	v_pk_mul_f32 v[68:69], v[68:69], s[18:19] op_sel_hi:[1,0]
	v_pk_mul_f32 v[62:63], v[62:63], s[18:19] op_sel_hi:[1,0]
	v_pk_mul_f32 v[64:65], v[64:65], s[18:19] op_sel_hi:[1,0]
	v_med3_f32 v98, v98, s57, v162
	v_med3_f32 v99, v99, s57, v162
	v_med3_f32 v100, v100, s57, v162
	v_med3_f32 v101, v101, s57, v162
	v_med3_f32 v94, v94, s57, v162
	v_med3_f32 v95, v95, s57, v162
	v_med3_f32 v96, v96, s57, v162
	v_med3_f32 v97, v97, s57, v162
	v_med3_f32 v66, v66, s57, v162
	v_med3_f32 v67, v67, s57, v162
	v_med3_f32 v68, v68, s57, v162
	v_med3_f32 v69, v69, s57, v162
	v_med3_f32 v62, v62, s57, v162
	v_med3_f32 v63, v63, s57, v162
	v_med3_f32 v64, v64, s57, v162
	v_med3_f32 v65, v65, s57, v162
	v_cvt_pk_fp8_f32 v244, v98, v99
	v_cvt_pk_fp8_f32 v245, v94, v95
	v_cvt_pk_fp8_f32 v246, v66, v67
	v_cvt_pk_fp8_f32 v247, v62, v63
	v_lshl_add_u64 v[238:239], s[8:9], 0, v[234:235]
	v_cvt_pk_fp8_f32 v244, v100, v101 op_sel:[0,0,1]
	v_cvt_pk_fp8_f32 v245, v96, v97 op_sel:[0,0,1]
	v_cvt_pk_fp8_f32 v246, v68, v69 op_sel:[0,0,1]
	v_cvt_pk_fp8_f32 v247, v64, v65 op_sel:[0,0,1]
	v_lshl_add_u64 v[238:239], v[238:239], 0, s[4:5]
	v_lshl_add_u64 v[238:239], v[238:239], 0, v[232:233]
	s_nop 1
	v_permlane16_swap_b32_e32 v244, v246
	v_permlane16_swap_b32_e32 v245, v247
	s_nop 0
	global_store_dwordx4 v[238:239], v[244:247], off
	v_or_b32_e32 v234, 128, v140
	v_ashrrev_i32_e32 v235, 31, v234
	v_lshlrev_b64 v[234:235], 10, v[234:235]
	v_pk_mul_f32 v[74:75], v[74:75], s[16:17] op_sel_hi:[1,0]
	v_pk_mul_f32 v[76:77], v[76:77], s[16:17] op_sel_hi:[1,0]
	v_pk_mul_f32 v[70:71], v[70:71], s[16:17] op_sel_hi:[1,0]
	v_pk_mul_f32 v[72:73], v[72:73], s[16:17] op_sel_hi:[1,0]
	v_pk_mul_f32 v[42:43], v[42:43], s[16:17] op_sel_hi:[1,0]
	v_pk_mul_f32 v[44:45], v[44:45], s[16:17] op_sel_hi:[1,0]
	v_pk_mul_f32 v[38:39], v[38:39], s[16:17] op_sel_hi:[1,0]
	v_pk_mul_f32 v[40:41], v[40:41], s[16:17] op_sel_hi:[1,0]
	v_med3_f32 v74, v74, s57, v162
	v_med3_f32 v75, v75, s57, v162
	v_med3_f32 v76, v76, s57, v162
	v_med3_f32 v77, v77, s57, v162
	v_med3_f32 v70, v70, s57, v162
	v_med3_f32 v71, v71, s57, v162
	v_med3_f32 v72, v72, s57, v162
	v_med3_f32 v73, v73, s57, v162
	v_med3_f32 v42, v42, s57, v162
	v_med3_f32 v43, v43, s57, v162
	v_med3_f32 v44, v44, s57, v162
	v_med3_f32 v45, v45, s57, v162
	v_med3_f32 v38, v38, s57, v162
	v_med3_f32 v39, v39, s57, v162
	v_med3_f32 v40, v40, s57, v162
	v_med3_f32 v41, v41, s57, v162
	v_cvt_pk_fp8_f32 v240, v74, v75
	v_cvt_pk_fp8_f32 v241, v70, v71
	v_cvt_pk_fp8_f32 v242, v42, v43
	v_cvt_pk_fp8_f32 v243, v38, v39
	v_lshl_add_u64 v[236:237], s[10:11], 0, v[234:235]
	v_cvt_pk_fp8_f32 v240, v76, v77 op_sel:[0,0,1]
	v_cvt_pk_fp8_f32 v241, v72, v73 op_sel:[0,0,1]
	v_cvt_pk_fp8_f32 v242, v44, v45 op_sel:[0,0,1]
	v_cvt_pk_fp8_f32 v243, v40, v41 op_sel:[0,0,1]
	v_lshl_add_u64 v[236:237], v[236:237], 0, s[4:5]
	v_lshl_add_u64 v[236:237], v[236:237], 0, v[232:233]
	s_nop 1
	v_permlane16_swap_b32_e32 v240, v242
	v_permlane16_swap_b32_e32 v241, v243
	s_nop 0
	global_store_dwordx4 v[236:237], v[240:243], off
	v_pk_mul_f32 v[82:83], v[82:83], s[18:19] op_sel_hi:[1,0]
	v_pk_mul_f32 v[84:85], v[84:85], s[18:19] op_sel_hi:[1,0]
	v_pk_mul_f32 v[78:79], v[78:79], s[18:19] op_sel_hi:[1,0]
	v_pk_mul_f32 v[80:81], v[80:81], s[18:19] op_sel_hi:[1,0]
	v_pk_mul_f32 v[50:51], v[50:51], s[18:19] op_sel_hi:[1,0]
	v_pk_mul_f32 v[52:53], v[52:53], s[18:19] op_sel_hi:[1,0]
	v_pk_mul_f32 v[46:47], v[46:47], s[18:19] op_sel_hi:[1,0]
	v_pk_mul_f32 v[48:49], v[48:49], s[18:19] op_sel_hi:[1,0]
	v_med3_f32 v82, v82, s57, v162
	v_med3_f32 v83, v83, s57, v162
	v_med3_f32 v84, v84, s57, v162
	v_med3_f32 v85, v85, s57, v162
	v_med3_f32 v78, v78, s57, v162
	v_med3_f32 v79, v79, s57, v162
	v_med3_f32 v80, v80, s57, v162
	v_med3_f32 v81, v81, s57, v162
	v_med3_f32 v50, v50, s57, v162
	v_med3_f32 v51, v51, s57, v162
	v_med3_f32 v52, v52, s57, v162
	v_med3_f32 v53, v53, s57, v162
	v_med3_f32 v46, v46, s57, v162
	v_med3_f32 v47, v47, s57, v162
	v_med3_f32 v48, v48, s57, v162
	v_med3_f32 v49, v49, s57, v162
	v_cvt_pk_fp8_f32 v244, v82, v83
	v_cvt_pk_fp8_f32 v245, v78, v79
	v_cvt_pk_fp8_f32 v246, v50, v51
	v_cvt_pk_fp8_f32 v247, v46, v47
	v_lshl_add_u64 v[238:239], s[8:9], 0, v[234:235]
	v_cvt_pk_fp8_f32 v244, v84, v85 op_sel:[0,0,1]
	v_cvt_pk_fp8_f32 v245, v80, v81 op_sel:[0,0,1]
	v_cvt_pk_fp8_f32 v246, v52, v53 op_sel:[0,0,1]
	v_cvt_pk_fp8_f32 v247, v48, v49 op_sel:[0,0,1]
	v_lshl_add_u64 v[238:239], v[238:239], 0, s[4:5]
	v_lshl_add_u64 v[238:239], v[238:239], 0, v[232:233]
	s_nop 1
	v_permlane16_swap_b32_e32 v244, v246
	v_permlane16_swap_b32_e32 v245, v247
	s_nop 0
	global_store_dwordx4 v[238:239], v[244:247], off
	v_or_b32_e32 v234, 160, v140
	v_ashrrev_i32_e32 v235, 31, v234
	v_lshlrev_b64 v[234:235], 10, v[234:235]
	v_pk_mul_f32 v[26:27], v[26:27], s[16:17] op_sel_hi:[1,0]
	v_pk_mul_f32 v[28:29], v[28:29], s[16:17] op_sel_hi:[1,0]
	v_pk_mul_f32 v[22:23], v[22:23], s[16:17] op_sel_hi:[1,0]
	v_pk_mul_f32 v[24:25], v[24:25], s[16:17] op_sel_hi:[1,0]
	v_pk_mul_f32 v[10:11], v[10:11], s[16:17] op_sel_hi:[1,0]
	v_pk_mul_f32 v[12:13], v[12:13], s[16:17] op_sel_hi:[1,0]
	v_pk_mul_f32 v[6:7], v[6:7], s[16:17] op_sel_hi:[1,0]
	v_pk_mul_f32 v[8:9], v[8:9], s[16:17] op_sel_hi:[1,0]
	v_med3_f32 v26, v26, s57, v162
	v_med3_f32 v27, v27, s57, v162
	v_med3_f32 v28, v28, s57, v162
	v_med3_f32 v29, v29, s57, v162
	v_med3_f32 v22, v22, s57, v162
	v_med3_f32 v23, v23, s57, v162
	v_med3_f32 v24, v24, s57, v162
	v_med3_f32 v25, v25, s57, v162
	v_med3_f32 v10, v10, s57, v162
	v_med3_f32 v11, v11, s57, v162
	v_med3_f32 v12, v12, s57, v162
	v_med3_f32 v13, v13, s57, v162
	v_med3_f32 v6, v6, s57, v162
	v_med3_f32 v7, v7, s57, v162
	v_med3_f32 v8, v8, s57, v162
	v_med3_f32 v9, v9, s57, v162
	v_cvt_pk_fp8_f32 v240, v26, v27
	v_cvt_pk_fp8_f32 v241, v22, v23
	v_cvt_pk_fp8_f32 v242, v10, v11
	v_cvt_pk_fp8_f32 v243, v6, v7
	v_lshl_add_u64 v[236:237], s[10:11], 0, v[234:235]
	v_cvt_pk_fp8_f32 v240, v28, v29 op_sel:[0,0,1]
	v_cvt_pk_fp8_f32 v241, v24, v25 op_sel:[0,0,1]
	v_cvt_pk_fp8_f32 v242, v12, v13 op_sel:[0,0,1]
	v_cvt_pk_fp8_f32 v243, v8, v9 op_sel:[0,0,1]
	v_lshl_add_u64 v[236:237], v[236:237], 0, s[4:5]
	v_lshl_add_u64 v[236:237], v[236:237], 0, v[232:233]
	s_nop 1
	v_permlane16_swap_b32_e32 v240, v242
	v_permlane16_swap_b32_e32 v241, v243
	s_nop 0
	global_store_dwordx4 v[236:237], v[240:243], off
	v_pk_mul_f32 v[34:35], v[34:35], s[18:19] op_sel_hi:[1,0]
	v_pk_mul_f32 v[36:37], v[36:37], s[18:19] op_sel_hi:[1,0]
	v_pk_mul_f32 v[30:31], v[30:31], s[18:19] op_sel_hi:[1,0]
	v_pk_mul_f32 v[32:33], v[32:33], s[18:19] op_sel_hi:[1,0]
	v_pk_mul_f32 v[18:19], v[18:19], s[18:19] op_sel_hi:[1,0]
	v_pk_mul_f32 v[20:21], v[20:21], s[18:19] op_sel_hi:[1,0]
	v_pk_mul_f32 v[14:15], v[14:15], s[18:19] op_sel_hi:[1,0]
	v_pk_mul_f32 v[16:17], v[16:17], s[18:19] op_sel_hi:[1,0]
	v_med3_f32 v34, v34, s57, v162
	v_med3_f32 v35, v35, s57, v162
	v_med3_f32 v36, v36, s57, v162
	v_med3_f32 v37, v37, s57, v162
	v_med3_f32 v30, v30, s57, v162
	v_med3_f32 v31, v31, s57, v162
	v_med3_f32 v32, v32, s57, v162
	v_med3_f32 v33, v33, s57, v162
	v_med3_f32 v18, v18, s57, v162
	v_med3_f32 v19, v19, s57, v162
	v_med3_f32 v20, v20, s57, v162
	v_med3_f32 v21, v21, s57, v162
	v_med3_f32 v14, v14, s57, v162
	v_med3_f32 v15, v15, s57, v162
	v_med3_f32 v16, v16, s57, v162
	v_med3_f32 v17, v17, s57, v162
	v_cvt_pk_fp8_f32 v244, v34, v35
	v_cvt_pk_fp8_f32 v245, v30, v31
	v_cvt_pk_fp8_f32 v246, v18, v19
	v_cvt_pk_fp8_f32 v247, v14, v15
	v_lshl_add_u64 v[238:239], s[8:9], 0, v[234:235]
	v_cvt_pk_fp8_f32 v244, v36, v37 op_sel:[0,0,1]
	v_cvt_pk_fp8_f32 v245, v32, v33 op_sel:[0,0,1]
	v_cvt_pk_fp8_f32 v246, v20, v21 op_sel:[0,0,1]
	v_cvt_pk_fp8_f32 v247, v16, v17 op_sel:[0,0,1]
	v_lshl_add_u64 v[238:239], v[238:239], 0, s[4:5]
	v_lshl_add_u64 v[238:239], v[238:239], 0, v[232:233]
	s_nop 1
	v_permlane16_swap_b32_e32 v244, v246
	v_permlane16_swap_b32_e32 v245, v247
	s_nop 0
	global_store_dwordx4 v[238:239], v[244:247], off
	v_readlane_b32 s40, v254, 42
	s_add_i32 s54, s54, s40
	s_andn2_b64 vcc, exec, s[0:1]
	s_mov_b32 s59, s28
	s_mov_b32 s38, s30
	s_mov_b64 s[44:45], s[36:37]
	s_mov_b64 s[42:43], s[34:35]
	v_readlane_b32 s41, v254, 43
	s_cbranch_vccz .LBB0_954
